# compaction fast path: batched compares into SGPR pairs, scalar popcounts/prefix, mbcnt positions, masked ds_write_b16; original code kept as overflow fallback (on top of v47)
# baseline (speedup 1.0000x reference)
.LBB0_833:
	s_mov_b64 s[12:13], exec
	s_mov_b32 s10, 0
	v_cmp_le_u32_e64 s[14:15], s9, v90
	v_cmp_le_u32_e64 s[16:17], s9, v88
	v_cmp_le_u32_e64 s[18:19], s9, v89
	v_cmp_le_u32_e64 s[20:21], s9, v86
	v_cmp_le_u32_e64 s[22:23], s9, v87
	v_cmp_le_u32_e64 s[24:25], s9, v84
	v_cmp_le_u32_e64 s[26:27], s9, v85
	v_cmp_le_u32_e64 s[28:29], s9, v82
	v_cmp_le_u32_e64 s[30:31], s9, v83
	v_cmp_le_u32_e64 s[34:35], s9, v80
	v_cmp_le_u32_e64 s[36:37], s9, v81
	v_cmp_le_u32_e64 s[38:39], s9, v9
	s_bcnt1_i32_b64 s40, s[14:15]
	s_bcnt1_i32_b64 s41, s[16:17]
	s_bcnt1_i32_b64 s42, s[18:19]
	s_bcnt1_i32_b64 s43, s[20:21]
	s_bcnt1_i32_b64 s46, s[22:23]
	s_bcnt1_i32_b64 s47, s[24:25]
	s_add_i32 s0, s10, s40
	s_add_i32 s0, s0, s41
	s_add_i32 s0, s0, s42
	s_add_i32 s0, s0, s43
	s_add_i32 s0, s0, s46
	s_add_i32 s0, s0, s47
	s_cmpk_gt_u32 s0, 0x100
	s_cbranch_scc1 .Lcomp_slow
	s_lshl_b32 s1, s10, 1
	s_add_i32 s1, s1, s95
	s_mov_b64 exec, s[14:15]
	v_mbcnt_lo_u32_b32 v79, s14, 0
	v_mbcnt_hi_u32_b32 v79, s15, v79
	v_lshl_add_u32 v79, v79, 1, s1
	v_xor_b32_e32 v91, -1, v90
	ds_write_b16 v79, v91
	s_add_i32 s10, s10, s40
	s_lshl_b32 s1, s10, 1
	s_add_i32 s1, s1, s95
	s_mov_b64 exec, s[16:17]
	v_mbcnt_lo_u32_b32 v79, s16, 0
	v_mbcnt_hi_u32_b32 v79, s17, v79
	v_lshl_add_u32 v79, v79, 1, s1
	v_xor_b32_e32 v91, -1, v88
	ds_write_b16 v79, v91
	s_add_i32 s10, s10, s41
	s_lshl_b32 s1, s10, 1
	s_add_i32 s1, s1, s95
	s_mov_b64 exec, s[18:19]
	v_mbcnt_lo_u32_b32 v79, s18, 0
	v_mbcnt_hi_u32_b32 v79, s19, v79
	v_lshl_add_u32 v79, v79, 1, s1
	v_xor_b32_e32 v91, -1, v89
	ds_write_b16 v79, v91
	s_add_i32 s10, s10, s42
	s_lshl_b32 s1, s10, 1
	s_add_i32 s1, s1, s95
	s_mov_b64 exec, s[20:21]
	v_mbcnt_lo_u32_b32 v79, s20, 0
	v_mbcnt_hi_u32_b32 v79, s21, v79
	v_lshl_add_u32 v79, v79, 1, s1
	v_xor_b32_e32 v91, -1, v86
	ds_write_b16 v79, v91
	s_add_i32 s10, s10, s43
	s_lshl_b32 s1, s10, 1
	s_add_i32 s1, s1, s95
	s_mov_b64 exec, s[22:23]
	v_mbcnt_lo_u32_b32 v79, s22, 0
	v_mbcnt_hi_u32_b32 v79, s23, v79
	v_lshl_add_u32 v79, v79, 1, s1
	v_xor_b32_e32 v91, -1, v87
	ds_write_b16 v79, v91
	s_add_i32 s10, s10, s46
	s_lshl_b32 s1, s10, 1
	s_add_i32 s1, s1, s95
	s_mov_b64 exec, s[24:25]
	v_mbcnt_lo_u32_b32 v79, s24, 0
	v_mbcnt_hi_u32_b32 v79, s25, v79
	v_lshl_add_u32 v79, v79, 1, s1
	v_xor_b32_e32 v91, -1, v84
	ds_write_b16 v79, v91
	s_add_i32 s10, s10, s47
	s_mov_b64 exec, s[12:13]
	s_bcnt1_i32_b64 s40, s[26:27]
	s_bcnt1_i32_b64 s41, s[28:29]
	s_bcnt1_i32_b64 s42, s[30:31]
	s_bcnt1_i32_b64 s43, s[34:35]
	s_bcnt1_i32_b64 s46, s[36:37]
	s_bcnt1_i32_b64 s47, s[38:39]
	s_add_i32 s0, s10, s40
	s_add_i32 s0, s0, s41
	s_add_i32 s0, s0, s42
	s_add_i32 s0, s0, s43
	s_add_i32 s0, s0, s46
	s_add_i32 s0, s0, s47
	s_cmpk_gt_u32 s0, 0x100
	s_cbranch_scc1 .Lcomp_slow
	s_lshl_b32 s1, s10, 1
	s_add_i32 s1, s1, s95
	s_mov_b64 exec, s[26:27]
	v_mbcnt_lo_u32_b32 v79, s26, 0
	v_mbcnt_hi_u32_b32 v79, s27, v79
	v_lshl_add_u32 v79, v79, 1, s1
	v_xor_b32_e32 v91, -1, v85
	ds_write_b16 v79, v91
	s_add_i32 s10, s10, s40
	s_lshl_b32 s1, s10, 1
	s_add_i32 s1, s1, s95
	s_mov_b64 exec, s[28:29]
	v_mbcnt_lo_u32_b32 v79, s28, 0
	v_mbcnt_hi_u32_b32 v79, s29, v79
	v_lshl_add_u32 v79, v79, 1, s1
	v_xor_b32_e32 v91, -1, v82
	ds_write_b16 v79, v91
	s_add_i32 s10, s10, s41
	s_lshl_b32 s1, s10, 1
	s_add_i32 s1, s1, s95
	s_mov_b64 exec, s[30:31]
	v_mbcnt_lo_u32_b32 v79, s30, 0
	v_mbcnt_hi_u32_b32 v79, s31, v79
	v_lshl_add_u32 v79, v79, 1, s1
	v_xor_b32_e32 v91, -1, v83
	ds_write_b16 v79, v91
	s_add_i32 s10, s10, s42
	s_lshl_b32 s1, s10, 1
	s_add_i32 s1, s1, s95
	s_mov_b64 exec, s[34:35]
	v_mbcnt_lo_u32_b32 v79, s34, 0
	v_mbcnt_hi_u32_b32 v79, s35, v79
	v_lshl_add_u32 v79, v79, 1, s1
	v_xor_b32_e32 v91, -1, v80
	ds_write_b16 v79, v91
	s_add_i32 s10, s10, s43
	s_lshl_b32 s1, s10, 1
	s_add_i32 s1, s1, s95
	s_mov_b64 exec, s[36:37]
	v_mbcnt_lo_u32_b32 v79, s36, 0
	v_mbcnt_hi_u32_b32 v79, s37, v79
	v_lshl_add_u32 v79, v79, 1, s1
	v_xor_b32_e32 v91, -1, v81
	ds_write_b16 v79, v91
	s_add_i32 s10, s10, s46
	s_lshl_b32 s1, s10, 1
	s_add_i32 s1, s1, s95
	s_mov_b64 exec, s[38:39]
	v_mbcnt_lo_u32_b32 v79, s38, 0
	v_mbcnt_hi_u32_b32 v79, s39, v79
	v_lshl_add_u32 v79, v79, 1, s1
	v_xor_b32_e32 v91, -1, v9
	ds_write_b16 v79, v91
	s_add_i32 s10, s10, s47
	s_mov_b64 exec, s[12:13]
	s_cmp_lt_u32 s8, 13
	s_cbranch_scc1 .LBB0_920
	v_cmp_le_u32_e64 s[14:15], s9, v78
	v_cmp_le_u32_e64 s[16:17], s9, v7
	v_cmp_le_u32_e64 s[18:19], s9, v8
	v_cmp_le_u32_e64 s[20:21], s9, v5
	v_cmp_le_u32_e64 s[22:23], s9, v6
	v_cmp_le_u32_e64 s[24:25], s9, v3
	v_cmp_le_u32_e64 s[26:27], s9, v4
	v_cmp_le_u32_e64 s[28:29], s9, v2
	s_bcnt1_i32_b64 s40, s[14:15]
	s_bcnt1_i32_b64 s41, s[16:17]
	s_bcnt1_i32_b64 s42, s[18:19]
	s_bcnt1_i32_b64 s43, s[20:21]
	s_bcnt1_i32_b64 s46, s[22:23]
	s_bcnt1_i32_b64 s47, s[24:25]
	s_add_i32 s0, s10, s40
	s_add_i32 s0, s0, s41
	s_add_i32 s0, s0, s42
	s_add_i32 s0, s0, s43
	s_add_i32 s0, s0, s46
	s_add_i32 s0, s0, s47
	s_cmpk_gt_u32 s0, 0x100
	s_cbranch_scc1 .Lcomp_slow
	s_lshl_b32 s1, s10, 1
	s_add_i32 s1, s1, s95
	s_mov_b64 exec, s[14:15]
	v_mbcnt_lo_u32_b32 v79, s14, 0
	v_mbcnt_hi_u32_b32 v79, s15, v79
	v_lshl_add_u32 v79, v79, 1, s1
	v_xor_b32_e32 v91, -1, v78
	ds_write_b16 v79, v91
	s_add_i32 s10, s10, s40
	s_lshl_b32 s1, s10, 1
	s_add_i32 s1, s1, s95
	s_mov_b64 exec, s[16:17]
	v_mbcnt_lo_u32_b32 v79, s16, 0
	v_mbcnt_hi_u32_b32 v79, s17, v79
	v_lshl_add_u32 v79, v79, 1, s1
	v_xor_b32_e32 v91, -1, v7
	ds_write_b16 v79, v91
	s_add_i32 s10, s10, s41
	s_lshl_b32 s1, s10, 1
	s_add_i32 s1, s1, s95
	s_mov_b64 exec, s[18:19]
	v_mbcnt_lo_u32_b32 v79, s18, 0
	v_mbcnt_hi_u32_b32 v79, s19, v79
	v_lshl_add_u32 v79, v79, 1, s1
	v_xor_b32_e32 v91, -1, v8
	ds_write_b16 v79, v91
	s_add_i32 s10, s10, s42
	s_lshl_b32 s1, s10, 1
	s_add_i32 s1, s1, s95
	s_mov_b64 exec, s[20:21]
	v_mbcnt_lo_u32_b32 v79, s20, 0
	v_mbcnt_hi_u32_b32 v79, s21, v79
	v_lshl_add_u32 v79, v79, 1, s1
	v_xor_b32_e32 v91, -1, v5
	ds_write_b16 v79, v91
	s_add_i32 s10, s10, s43
	s_lshl_b32 s1, s10, 1
	s_add_i32 s1, s1, s95
	s_mov_b64 exec, s[22:23]
	v_mbcnt_lo_u32_b32 v79, s22, 0
	v_mbcnt_hi_u32_b32 v79, s23, v79
	v_lshl_add_u32 v79, v79, 1, s1
	v_xor_b32_e32 v91, -1, v6
	ds_write_b16 v79, v91
	s_add_i32 s10, s10, s46
	s_lshl_b32 s1, s10, 1
	s_add_i32 s1, s1, s95
	s_mov_b64 exec, s[24:25]
	v_mbcnt_lo_u32_b32 v79, s24, 0
	v_mbcnt_hi_u32_b32 v79, s25, v79
	v_lshl_add_u32 v79, v79, 1, s1
	v_xor_b32_e32 v91, -1, v3
	ds_write_b16 v79, v91
	s_add_i32 s10, s10, s47
	s_mov_b64 exec, s[12:13]
	s_cmp_lt_u32 s8, 19
	s_cbranch_scc1 .LBB0_920
	s_bcnt1_i32_b64 s40, s[26:27]
	s_bcnt1_i32_b64 s41, s[28:29]
	s_add_i32 s0, s10, s40
	s_add_i32 s0, s0, s41
	s_cmpk_gt_u32 s0, 0x100
	s_cbranch_scc1 .Lcomp_slow
	s_lshl_b32 s1, s10, 1
	s_add_i32 s1, s1, s95
	s_mov_b64 exec, s[26:27]
	v_mbcnt_lo_u32_b32 v79, s26, 0
	v_mbcnt_hi_u32_b32 v79, s27, v79
	v_lshl_add_u32 v79, v79, 1, s1
	v_xor_b32_e32 v91, -1, v4
	ds_write_b16 v79, v91
	s_add_i32 s10, s10, s40
	s_lshl_b32 s1, s10, 1
	s_add_i32 s1, s1, s95
	s_mov_b64 exec, s[28:29]
	v_mbcnt_lo_u32_b32 v79, s28, 0
	v_mbcnt_hi_u32_b32 v79, s29, v79
	v_lshl_add_u32 v79, v79, 1, s1
	v_xor_b32_e32 v91, -1, v2
	ds_write_b16 v79, v91
	s_add_i32 s10, s10, s41
	s_mov_b64 exec, s[12:13]
	s_branch .LBB0_920
.Lcomp_slow:
	s_mov_b64 exec, s[12:13]
	s_cmp_eq_u32 s8, 0
	s_mov_b32 s10, 0
	s_cbranch_scc1 .LBB0_880

.LBB0_879:
	s_mov_b32 s9, s10
	s_branch .LBB0_833
